# attention phase: static s_setprio 1 for waves 0-3 (reset at phase end), on top of the nt stream hints
# baseline (speedup 1.0000x reference)
; #define GAS __attribute__((address_space(1)))
; #define PHASE_FRAME(F0) Frame F = F0; { int t_ = threadIdx.x; asm volatile("" : "+v"(t_)); F.tid = t_; F.lane = t_ & 63; F.wave = __builtin_amdgcn_readfirstlane(t_ >> 6); }
; __device__ __forceinline__ void att_fast_phase(const Frame& F0, int jl) {
;     PHASE_FRAME(F0);
;     const attn_body::bf16* Q = (const attn_body::bf16*)(F.ws + WS_Q); const attn_body::bf16* K = (const attn_body::bf16*)(F.ws + WS_K); const attn_body::bf16* V = (const attn_body::bf16*)(F.ws + WS_V);
;     const float skv = F.lane < 8 ? ((const GAS float*)(inp(F, I_SINK) + jl * 8))[F.lane] * LOG2E : -INFINITY;
;     for (int i = 0;; ++i) {
;         const int lin = i * F.G + (int)blockIdx.x; if (lin >= 2304) break;
;         const int slot = lin >> 8; int v = lin & 255; if (F.G == 256) v = (v & 7) * 32 + (v >> 3);
;         attn_body::AttU U;
;         U.wqm = 7; U.whs = 3; U.hs = 8; U.skv = skv;
; __global__ void __launch_bounds__(512, 2) mk_fwd(Args args) {
;     ...
;                 att_fast_phase(F, jl);
.LBB0_893:
	s_or_b64 exec, exec, s[0:1]
	v_readlane_b32 s0, v253, 58
	v_readlane_b32 s1, v253, 59
	s_andn2_b64 vcc, exec, s[0:1]
	s_cbranch_vccnz .LBB0_995
	v_readfirstlane_b32 s10, v0
	s_nop 3
	s_lshr_b32 s10, s10, 8
	s_cmp_eq_u32 s10, 0
	s_cbranch_scc0 .Lattprio
	s_setprio 1
.Lattprio:
	s_mov_b32 s10, 0
	s_mov_b32 s17, s84
	s_branch .LBB0_896

; #define SEAM(k) do { } while (0)
; #define SEAM(k) do { if (IN(k) && IN((k) + 1)) xcd_barrier(bar); } while (0)
; __device__ __forceinline__ void xcd_barrier(const XcdBarrier& b) {
;     asm volatile("s_waitcnt vmcnt(0)" ::: "memory");
;     __syncthreads();
;     if (threadIdx.x == 0) {
;         unsigned* bar = b.bar;
;         __builtin_amdgcn_s_waitcnt(0);
;         unsigned nloc = b.st[0], nx = b.st[1];
;         if (nloc == 0u) { xcd_barrier_complete(bar, b.x, nloc, nx); b.st[0] = nloc; b.st[1] = nx; }
; __global__ void __launch_bounds__(512, 2) mk_fwd(Args args) {
;     ...
;             SEAM(pb + 2);
.LBB0_995:
	s_setprio 0
	v_readlane_b32 s0, v255, 13
	s_or_b32 s0, s0, 4
	s_cmp_ge_i32 s0, s93
	s_cbranch_scc1 .LBB0_1049
	s_waitcnt vmcnt(0)
	s_barrier
	s_and_saveexec_b64 s[0:1], s[88:89]
	s_cbranch_execz .LBB0_1048
	v_readlane_b32 s2, v255, 3
	s_waitcnt vmcnt(0) expcnt(0) lgkmcnt(0)
	s_nop 0
	v_mov_b32_e32 v1, s2
	ds_read_b32 v3, v1
	v_readlane_b32 s2, v255, 4
	s_waitcnt lgkmcnt(0)
	v_cmp_ne_u32_e32 vcc, 0, v3
	v_mov_b32_e32 v1, s2
	ds_read_b32 v2, v1
	s_cbranch_vccnz .LBB0_1012
	s_load_dwordx2 s[2:3], s[86:87], 0x4
	s_mov_b32 s9, 1
	s_waitcnt lgkmcnt(0)
	s_mul_i32 s8, s2, s85
	s_mul_i32 s8, s8, s3
	s_branch .LBB0_1000
